# code placement: the out-/down-projection and in-projection K-loop heads moved to an 8-byte phase (one pad nop at each phase entry)
# speedup vs baseline: 1.0059x; 1.0029x over previous
; #define PG8_STAGE(bufoff, gbase, voff) do { _Pragma("unroll") for (int _i = 0; _i < 2; ++_i) \
;         __builtin_amdgcn_global_load_lds((const unsigned*)((const char*)(gbase) + (voff)[_i]), (PG8_LAS unsigned*)(lds + (bufoff) + ldsw + _i * 8192), 16, 0, 0); } while (0)
; #define PG8_WAIT_V(n) asm volatile("s_waitcnt vmcnt(" #n ")" ::: "memory")
; #define PG8_BAR __builtin_amdgcn_s_barrier()
; template <class Epi, class Sched, bool ALIGN_EPI = false, bool SP2 = false>
; __device__ __forceinline__ void gemm_phase(PG8_LAS unsigned char* lds, const Gemm g, const Sched& S, const Epi& E, const int tid) {
;     const int wid = __builtin_amdgcn_readfirstlane(tid >> 6), lane = tid & 63, wr = wid >> 2, wc = wid & 3, fr = lane & 15, fq = lane >> 4;
;     const int K = g.K, nt = K / BK;
;     unsigned voffA[2], voffB[2];
; #pragma unroll
;     for (int i = 0; i < 2; ++i) { int R, C; stage_rc(tid * 16 + i * 8192, R, C); const int Rb = Epi::PERM ? ((R & ~31) + perm32(R & 31)) : R;
;         voffA[i] = (unsigned)(R * g.lda + C) * 2u; voffB[i] = (unsigned)(Rb * K + C) * 2u; }
;     const size_t kstep = (size_t)(BK * 2);
;     const size_t hstep = (size_t)HALF * K * 2;
;     const size_t tstep = 2 * hstep;
;     const size_t hstepA = (size_t)HALF * g.lda * 2, tstepA = 2 * hstepA; const long padj = g.padj;
;     ...
;     const unsigned ldsw = (unsigned)wid * 1024u;
;     const int aoff = lds_byte(wr * 64 + fr, fq * 8), boff = lds_byte(wc * 32 + fr, fq * 8);
;     ...
;         PG8_WAIT_V(2); PG8_BAR;
;         PG8_STAGE(PG8_SB(1, 0), cB + kstep, voffB); PG8_STAGE(PG8_SA(1, 0), cA + kstep, voffA); PG8_STAGE(PG8_SB(1, 1), cB + hstep + kstep, voffB);
;         PG8_WAIT_V(6); PG8_BAR;
.LBB0_406:
	v_readlane_b32 s1, v254, 19
	v_mov_b32_e32 v199, v1
	v_mov_b32_e32 v203, v1
	s_cmp_lg_u32 s1, 12
	v_lshl_add_u64 v[8:9], s[26:27], 0, v[198:199]
	v_lshl_add_u64 v[12:13], s[8:9], 0, v[198:199]
	v_lshl_add_u64 v[14:15], s[8:9], 0, v[202:203]
	s_cselect_b64 s[8:9], -1, 0
	s_add_i32 s54, s47, 0x18000
	v_lshl_add_u64 v[10:11], s[26:27], 0, v[202:203]
	v_mov_b32_e32 v197, v1
	v_lshl_add_u64 v[8:9], v[8:9], 0, s[86:87]
	s_mov_b32 m0, s54
	s_add_i32 s55, s47, 0x1a000
	v_lshl_add_u64 v[16:17], s[28:29], 0, v[196:197]
	v_mov_b32_e32 v201, v1
	s_waitcnt vmcnt(2)
	s_barrier
	global_load_lds_dwordx4 v[8:9], off
	v_lshl_add_u64 v[8:9], v[10:11], 0, s[86:87]
	s_mov_b32 m0, s55
	s_add_i32 s56, s47, 0x8000
	v_lshl_add_u64 v[18:19], s[28:29], 0, v[200:201]
	global_load_lds_dwordx4 v[8:9], off
	v_lshl_add_u64 v[8:9], v[16:17], 0, s[86:87]
	s_mov_b32 m0, s56
	s_add_i32 s57, s47, 0xa000
	global_load_lds_dwordx4 v[8:9], off
	v_lshl_add_u64 v[8:9], v[18:19], 0, s[86:87]
	s_mov_b32 m0, s57
	s_add_i32 s58, s47, 0x1c000
	global_load_lds_dwordx4 v[8:9], off
	v_lshl_add_u64 v[8:9], v[12:13], 0, s[86:87]
	s_mov_b32 m0, s58
	s_add_i32 s59, s47, 0x1e000
	global_load_lds_dwordx4 v[8:9], off
	v_lshl_add_u64 v[8:9], v[14:15], 0, s[86:87]
	s_mov_b32 m0, s59
	v_bfe_u32 v7, v232, 4, 2
	global_load_lds_dwordx4 v[8:9], off
	v_and_b32_e32 v8, 15, v232
	v_lshlrev_b32_e32 v10, 4, v7
	v_lshl_or_b32 v195, s13, 6, v8
	v_lshl_or_b32 v8, v8, 6, v10
	v_lshlrev_b32_e32 v10, 2, v232
	s_and_b32 s60, s12, 3
	s_lshl_b32 s1, s13, 13
	v_and_b32_e32 v10, 32, v10
	v_bitop3_b32 v208, v8, s1, v10 bitop3:0xde
	s_lshl_b32 s1, s60, 12
	v_bitop3_b32 v209, s1, v8, v10 bitop3:0xf6
	v_and_b32_e32 v8, 64, v214
	v_lshlrev_b32_e32 v9, 3, v7
	v_cmp_eq_u32_e64 s[34:35], 0, v7
	v_xor_b32_e32 v7, 16, v214
	v_add_u32_e32 v8, 64, v8
	v_cmp_lt_i32_e32 vcc, v7, v8
	s_lshr_b32 s61, s11, 6
	s_cmpk_lt_u32 s10, 0x100
	v_cndmask_b32_e32 v7, v214, v7, vcc
	v_lshlrev_b32_e32 v211, 2, v7
	v_xor_b32_e32 v7, 32, v214
	v_cmp_lt_i32_e32 vcc, v7, v8
	v_readlane_b32 s1, v254, 12
	v_readlane_b32 s12, v254, 15
	v_cndmask_b32_e32 v7, v214, v7, vcc
	v_lshlrev_b32_e32 v212, 2, v7
	v_lshlrev_b32_e32 v7, 14, v4
	v_and_b32_e32 v7, 0xffff8000, v7
	v_lshl_add_u32 v5, v5, 11, v7
	v_and_b32_e32 v4, 1, v4
	v_lshl_or_b32 v4, v4, 6, v5
	s_cselect_b64 s[10:11], -1, 0
	s_ashr_i32 s63, s1, 31
	s_ashr_i32 s64, s12, 31
	v_lshl_add_u32 v204, v6, 1, v4
	v_lshlrev_b32_e32 v4, 14, v0
	v_readlane_b32 s13, v254, 16
	s_add_u32 s12, s74, 0x4000000
	v_and_b32_e32 v4, 0xffff8000, v4
	s_waitcnt vmcnt(6)
	s_addc_u32 s13, s75, 0
	v_lshl_add_u32 v2, v2, 11, v4
	v_and_b32_e32 v0, 1, v0
	s_add_u32 s14, s74, 0x3400000
	v_lshl_or_b32 v0, v0, 6, v2
	v_lshl_or_b32 v210, s60, 5, v9
	s_mov_b32 s62, 0
	s_addc_u32 s15, s75, 0
	v_mov_b32_e32 v205, v1
	v_lshl_add_u32 v206, v3, 1, v0
	v_mov_b32_e32 v207, v1
	s_barrier
	s_nop 0
	s_branch .LBB0_409

; #define PG8_STAGE(bufoff, gbase, voff) do { _Pragma("unroll") for (int _i = 0; _i < 2; ++_i) \
;         __builtin_amdgcn_global_load_lds((const unsigned*)((const char*)(gbase) + (voff)[_i]), (PG8_LAS unsigned*)(lds + (bufoff) + ldsw + _i * 8192), 16, 0, 0); } while (0)
; #define PG8_WAIT_V(n) asm volatile("s_waitcnt vmcnt(" #n ")" ::: "memory")
; #define PG8_BAR __builtin_amdgcn_s_barrier()
; template <class Epi, class Sched, bool ALIGN_EPI = false, bool SP2 = false>
; __device__ __forceinline__ void gemm_phase(PG8_LAS unsigned char* lds, const Gemm g, const Sched& S, const Epi& E, const int tid) {
;     const int wid = __builtin_amdgcn_readfirstlane(tid >> 6), lane = tid & 63, wr = wid >> 2, wc = wid & 3, fr = lane & 15, fq = lane >> 4;
;     const int K = g.K, nt = K / BK;
;     unsigned voffA[2], voffB[2];
; #pragma unroll
;     for (int i = 0; i < 2; ++i) { int R, C; stage_rc(tid * 16 + i * 8192, R, C); const int Rb = Epi::PERM ? ((R & ~31) + perm32(R & 31)) : R;
;         voffA[i] = (unsigned)(R * g.lda + C) * 2u; voffB[i] = (unsigned)(Rb * K + C) * 2u; }
;     const size_t kstep = (size_t)(BK * 2);
;     const size_t hstep = (size_t)HALF * K * 2;
;     const size_t tstep = 2 * hstep;
;     const size_t hstepA = (size_t)HALF * g.lda * 2, tstepA = 2 * hstepA; const long padj = g.padj;
;     ...
;     const unsigned ldsw = (unsigned)wid * 1024u;
;     const int aoff = lds_byte(wr * 64 + fr, fq * 8), boff = lds_byte(wc * 32 + fr, fq * 8);
;     ...
;         PG8_WAIT_V(2); PG8_BAR;
;         PG8_STAGE(PG8_SB(1, 0), cB + kstep, voffB); PG8_STAGE(PG8_SA(1, 0), cA + kstep, voffA); PG8_STAGE(PG8_SB(1, 1), cB + hstep + kstep, voffB);
;         PG8_WAIT_V(6); PG8_BAR;
.LBB0_550:
	v_readlane_b32 s6, v254, 20
	v_readlane_b32 s7, v254, 21
	s_ashr_i32 s7, s6, 31
	v_readlane_b32 s52, v253, 54
	s_lshl_b64 s[6:7], s[6:7], 2
	v_readlane_b32 s58, v253, 60
	v_mov_b32_e32 v149, v1
	v_readlane_b32 s59, v253, 61
	s_add_u32 s6, s58, s6
	v_lshl_add_u64 v[8:9], s[28:29], 0, v[148:149]
	v_mov_b32_e32 v153, v1
	v_readlane_b32 s53, v253, 55
	s_addc_u32 s7, s59, s7
	s_add_i32 s52, s44, 0x18000
	v_lshl_add_u64 v[10:11], s[28:29], 0, v[152:153]
	v_mov_b32_e32 v147, v1
	v_readlane_b32 s54, v253, 56
	v_readlane_b32 s55, v253, 57
	s_and_b32 s18, s10, 3
	v_lshl_add_u64 v[8:9], v[8:9], 0, s[86:87]
	s_mov_b32 m0, s52
	s_add_i32 s53, s44, 0x1a000
	v_lshl_add_u64 v[12:13], s[30:31], 0, v[146:147]
	v_mov_b32_e32 v151, v1
	s_lshl_b32 s14, s11, 6
	s_lshl_b32 s5, s11, 13
	s_lshl_b32 s9, s18, 12
	s_waitcnt vmcnt(2)
	s_barrier
	global_load_lds_dwordx4 v[8:9], off
	v_lshl_add_u64 v[8:9], v[10:11], 0, s[86:87]
	s_mov_b32 m0, s53
	s_add_i32 s54, s44, 0x8000
	s_add_i32 s55, s44, 0xa000
	v_lshl_add_u64 v[14:15], s[30:31], 0, v[150:151]
	v_readlane_b32 s56, v253, 58
	global_load_lds_dwordx4 v[8:9], off
	v_lshl_add_u64 v[8:9], v[12:13], 0, s[86:87]
	s_mov_b32 m0, s54
	s_add_u32 s12, s28, 0x40080
	v_readlane_b32 s57, v253, 59
	global_load_lds_dwordx4 v[8:9], off
	v_lshl_add_u64 v[8:9], v[14:15], 0, s[86:87]
	s_mov_b32 m0, s55
	s_addc_u32 s13, s29, 0
	s_add_i32 s56, s44, 0x1c000
	global_load_lds_dwordx4 v[8:9], off
	v_lshl_add_u64 v[8:9], s[12:13], 0, v[148:149]
	s_mov_b32 m0, s56
	s_add_i32 s57, s44, 0x1e000
	global_load_lds_dwordx4 v[8:9], off
	v_lshl_add_u64 v[8:9], s[12:13], 0, v[152:153]
	s_mov_b32 m0, s57
	v_lshrrev_b32_e32 v7, 4, v232
	global_load_lds_dwordx4 v[8:9], off
	v_and_b32_e32 v8, 15, v232
	v_bfe_u32 v9, v232, 4, 2
	v_lshlrev_b32_e32 v11, 4, v9
	v_lshlrev_b32_e32 v13, 2, v8
	v_lshlrev_b32_e32 v10, 3, v9
	v_lshl_or_b32 v12, v8, 6, v11
	v_and_b32_e32 v14, 32, v13
	s_cmpk_lt_u32 s8, 0x100
	v_bitop3_b32 v7, s10, v7, 3 bitop3:0xa8
	v_or_b32_e32 v163, s14, v8
	v_bitop3_b32 v167, s9, v12, v14 bitop3:0xf6
	s_cselect_b64 s[8:9], -1, 0
	v_cmp_eq_u32_e64 s[34:35], 0, v7
	s_lshl_b32 s10, s18, 7
	v_cmp_eq_u32_e64 s[36:37], 0, v8
	v_or_b32_e32 v7, s14, v10
	v_and_b32_e32 v8, 64, v214
	v_add_u32_e32 v171, s10, v7
	v_xor_b32_e32 v7, 32, v214
	v_add_u32_e32 v8, 64, v8
	v_cmp_lt_i32_e32 vcc, v7, v8
	v_or_b32_e32 v175, s10, v11
	s_lshl_b32 s10, s11, 8
	v_cndmask_b32_e32 v7, v214, v7, vcc
	v_lshlrev_b32_e32 v195, 2, v7
	v_xor_b32_e32 v7, 1, v214
	v_cmp_lt_i32_e32 vcc, v7, v8
	s_add_i32 s10, s10, 0x20200
	v_or_b32_e32 v181, s10, v13
	v_cndmask_b32_e32 v7, v214, v7, vcc
	v_lshlrev_b32_e32 v233, 2, v7
	v_xor_b32_e32 v7, 2, v214
	v_cmp_lt_i32_e32 vcc, v7, v8
	s_lshl_b32 s10, s18, 8
	s_add_i32 s10, s10, 0x22200
	v_cndmask_b32_e32 v7, v214, v7, vcc
	v_lshlrev_b32_e32 v234, 2, v7
	v_xor_b32_e32 v7, 4, v214
	v_cmp_lt_i32_e32 vcc, v7, v8
	v_lshl_or_b32 v187, v9, 5, s10
	s_add_u32 s10, s74, 0x18000000
	v_cndmask_b32_e32 v7, v214, v7, vcc
	v_lshlrev_b32_e32 v235, 2, v7
	v_xor_b32_e32 v7, 8, v214
	v_cmp_lt_i32_e32 vcc, v7, v8
	s_addc_u32 s11, s75, 0
	s_add_u32 s12, s74, 0x3600000
	v_cndmask_b32_e32 v7, v214, v7, vcc
	v_lshlrev_b32_e32 v236, 2, v7
	v_lshlrev_b32_e32 v7, 14, v4
	v_and_b32_e32 v7, 0xffff8000, v7
	v_lshl_add_u32 v5, v5, 11, v7
	v_and_b32_e32 v4, 1, v4
	v_lshl_or_b32 v4, v4, 6, v5
	s_addc_u32 s13, s75, 0
	v_lshl_add_u32 v154, v6, 1, v4
	v_lshlrev_b32_e32 v4, 14, v0
	s_add_u32 s14, s74, 0x8000000
	v_and_b32_e32 v4, 0xffff8000, v4
	s_waitcnt vmcnt(6)
	s_addc_u32 s15, s75, 0
	v_lshl_add_u32 v2, v2, 11, v4
	v_and_b32_e32 v0, 1, v0
	s_add_u32 s16, s74, 0x3700000
	v_lshl_or_b32 v0, v0, 6, v2
	v_bitop3_b32 v165, v12, s5, v14 bitop3:0xde
	s_mov_b32 s5, 0
	s_addc_u32 s17, s75, 0
	v_lshl_or_b32 v237, s18, 5, v10
	v_lshl_or_b32 v238, s18, 6, v10
	v_mov_b32_e32 v155, v1
	v_lshl_add_u32 v156, v3, 1, v0
	v_mov_b32_e32 v157, v1
	v_readlane_b32 s60, v253, 62
	v_readlane_b32 s61, v253, 63
	v_readlane_b32 s62, v254, 0
	v_readlane_b32 s63, v254, 1
	v_readlane_b32 s64, v254, 2
	v_readlane_b32 s65, v254, 3
	v_readlane_b32 s66, v254, 4
	v_readlane_b32 s67, v254, 5
	s_barrier
	s_nop 0
	s_branch .LBB0_553
